# speedup vs baseline: 1.0165x; 1.0165x over previous
.LBB1_33:
	s_or_b64 exec, exec, s[16:17]
	s_mul_i32 s17, s33, 0x9000
	s_add_i32 s18, s17, 0
	s_add_i32 s19, s18, 0x8000
	s_and_b32 s16, s40, 7
	v_lshl_add_u32 v66, v207, 4, s19
	s_cmp_lg_u32 s16, 0
	v_lshl_add_u32 v231, v1, 4, v66
	s_cbranch_scc1 .LBB1_35
	ds_read_b128 v[2:5], v231 offset:33280
	ds_read_b128 v[6:9], v231 offset:33312
	ds_read_b128 v[10:13], v231 offset:33344
	ds_read_b128 v[14:17], v231 offset:33376
	ds_read_b128 v[18:21], v231 offset:33408
	ds_read_b128 v[22:25], v231 offset:33440
	ds_read_b128 v[26:29], v231 offset:33472
	ds_read_b128 v[30:33], v231 offset:33504
	ds_read_b128 v[34:37], v231 offset:33536
	ds_read_b128 v[38:41], v231 offset:33568
	ds_read_b128 v[42:45], v231 offset:33600
	ds_read_b128 v[46:49], v231 offset:33632
	ds_read_b128 v[50:53], v231 offset:33664
	ds_read_b128 v[54:57], v231 offset:33696
	ds_read_b128 v[58:61], v231 offset:33728
	ds_read_b128 v[62:65], v231 offset:33760
	s_waitcnt lgkmcnt(12)
	v_mfma_f32_32x32x16_f16 v[2:17], v[178:181], v[146:149], v[2:17]
	s_waitcnt lgkmcnt(8)
	v_mfma_f32_32x32x16_f16 v[18:33], v[178:181], v[154:157], v[18:33]
	s_waitcnt lgkmcnt(4)
	v_mfma_f32_32x32x16_f16 v[34:49], v[178:181], v[162:165], v[34:49]
	s_waitcnt lgkmcnt(0)
	v_mfma_f32_32x32x16_f16 v[50:65], v[178:181], v[170:173], v[50:65]
	v_mfma_f32_32x32x16_f16 v[2:17], v[182:185], v[150:153], v[2:17]
	v_mfma_f32_32x32x16_f16 v[18:33], v[182:185], v[158:161], v[18:33]
	v_mfma_f32_32x32x16_f16 v[34:49], v[182:185], v[166:169], v[34:49]
	v_mfma_f32_32x32x16_f16 v[50:65], v[182:185], v[174:177], v[50:65]
.LBB1_35:
	v_lshlrev_b32_e32 v66, 4, v227
	v_add3_u32 v82, s18, v66, v206
	ds_read_b128 v[66:69], v231 offset:32768
	ds_read_b128 v[70:73], v231 offset:32800
	ds_read_b128 v[74:77], v231 offset:32832
	ds_read_b128 v[78:81], v231 offset:32864
	ds_read_b128 v[190:193], v82 offset:32768
	ds_read_b128 v[194:197], v82 offset:33792
	ds_read_b128 v[198:201], v82 offset:34816
	ds_read_b128 v[202:205], v82 offset:35840
	ds_read_b128 v[212:215], v82 offset:36864
	ds_read_b128 v[232:235], v82 offset:37888
	ds_read_b128 v[236:239], v82 offset:38912
	ds_read_b128 v[240:243], v82 offset:39936
	s_waitcnt lgkmcnt(7)
	v_mfma_f32_32x32x16_f16 v[66:81], v[190:193], v[146:149], v[66:81]
	s_add_i32 s17, s17, 0xffff7000
	s_cmp_lg_u32 s33, 0
	s_cselect_b32 s17, s17, 0x12000
	s_waitcnt lgkmcnt(6)
	v_mfma_f32_32x32x16_f16 v[66:81], v[194:197], v[150:153], v[66:81]
	s_waitcnt lgkmcnt(5)
	v_mfma_f32_32x32x16_f16 v[66:81], v[198:201], v[154:157], v[66:81]
	s_waitcnt lgkmcnt(4)
	v_mfma_f32_32x32x16_f16 v[66:81], v[202:205], v[158:161], v[66:81]
	v_readfirstlane_b32 s18, v0
	s_lshl_b32 s20, s18, 4
	s_and_b32 s18, s20, 0xfffffc00
	s_add_i32 s17, s18, s17
	s_cmp_lg_u32 s3, -1
	s_cselect_b32 s18, s3, 0
	s_add_i32 s17, s17, s18
	s_add_u32 s18, s14, 0x372000
	s_addc_u32 s19, s15, 0
	s_mov_b32 m0, s17
	s_nop 0
	global_load_lds_dwordx4 v226, s[18:19]
	s_waitcnt lgkmcnt(3)
	v_mfma_f32_32x32x16_f16 v[66:81], v[212:215], v[162:165], v[66:81]
	s_add_u32 s18, s14, 0x374000
	s_addc_u32 s19, s15, 0
	s_add_i32 s21, s17, 0x2000
	s_mov_b32 m0, s21
	s_nop 0
	global_load_lds_dwordx4 v226, s[18:19]
	s_waitcnt lgkmcnt(2)
	v_mfma_f32_32x32x16_f16 v[66:81], v[232:235], v[166:169], v[66:81]
	s_add_u32 s18, s14, 0x376000
	s_addc_u32 s19, s15, 0
	s_add_i32 s21, s17, 0x4000
	s_mov_b32 m0, s21
	s_nop 0
	global_load_lds_dwordx4 v226, s[18:19]
	s_waitcnt lgkmcnt(1)
	v_mfma_f32_32x32x16_f16 v[66:81], v[236:239], v[170:173], v[66:81]
	s_add_u32 s18, s14, 0x378000
	s_addc_u32 s19, s15, 0
	s_add_i32 s21, s17, 0x6000
	s_mov_b32 m0, s21
	s_nop 0
	global_load_lds_dwordx4 v226, s[18:19]
	s_waitcnt lgkmcnt(0)
	v_mfma_f32_32x32x16_f16 v[66:81], v[240:243], v[174:177], v[66:81]
	s_add_u32 s18, s14, 0x37a000
	s_addc_u32 s19, s15, 0
	s_and_b32 s20, s20, 0xfffff000
	s_sub_i32 s17, s17, s20
	s_add_i32 s17, s17, 0x8000
	s_mov_b32 m0, s17
	s_nop 0
	global_load_lds_dwordx4 v224, s[18:19]
	ds_read_b128 v[190:193], v82 offset:40960
	ds_read_b128 v[194:197], v82 offset:41984
	ds_read_b128 v[198:201], v82 offset:43008
	ds_read_b128 v[202:205], v82 offset:44032
	ds_read_b128 v[212:215], v82 offset:45056
	ds_read_b128 v[232:235], v82 offset:46080
	ds_read_b128 v[236:239], v82 offset:47104
	ds_read_b128 v[240:243], v82 offset:48128
	v_cvt_pk_f16_f32 v66, v66, v67
	v_cvt_pk_f16_f32 v67, v68, v69
	v_cvt_pk_f16_f32 v68, v70, v71
	v_cvt_pk_f16_f32 v69, v72, v73
	v_and_b32_e32 v70, 0x7fff7fff, v66
	v_and_b32_e32 v71, 0x7fff7fff, v67
	v_and_b32_e32 v72, 0x7fff7fff, v68
	v_and_b32_e32 v73, 0x7fff7fff, v69
	v_pk_min_f16 v70, v70, v229
	v_pk_min_f16 v71, v71, v229
	v_pk_min_f16 v72, v72, v229
	v_pk_min_f16 v73, v73, v229
	v_pk_max_f16 v66, v66, v228
	v_pk_max_f16 v67, v67, v228
	s_nop 0
	v_pk_fma_f16 v70, v70, s26, -1.0 op_sel_hi:[1,0,0]
	v_pk_fma_f16 v71, v71, s26, -1.0 op_sel_hi:[1,0,0]
	v_pk_fma_f16 v72, v72, s26, -1.0 op_sel_hi:[1,0,0]
	v_pk_fma_f16 v73, v73, s26, -1.0 op_sel_hi:[1,0,0]
	v_pk_fma_f16 v82, v70, s27, v230 op_sel_hi:[1,0,0]
	v_pk_fma_f16 v83, v71, s27, v230 op_sel_hi:[1,0,0]
	v_pk_fma_f16 v144, v72, s27, v230 op_sel_hi:[1,0,0]
	v_pk_fma_f16 v145, v73, s27, v230 op_sel_hi:[1,0,0]
	v_pk_fma_f16 v82, v70, v82, s28 op_sel_hi:[1,1,0]
	v_pk_fma_f16 v83, v71, v83, s28 op_sel_hi:[1,1,0]
	v_pk_fma_f16 v144, v72, v144, s28 op_sel_hi:[1,1,0]
	v_pk_fma_f16 v145, v73, v145, s28 op_sel_hi:[1,1,0]
	v_pk_fma_f16 v82, v70, v82, s29 op_sel_hi:[1,1,0]
	v_pk_fma_f16 v83, v71, v83, s29 op_sel_hi:[1,1,0]
	v_pk_fma_f16 v144, v72, v144, s29 op_sel_hi:[1,1,0]
	v_pk_fma_f16 v145, v73, v145, s29 op_sel_hi:[1,1,0]
	v_pk_fma_f16 v82, v70, v82, s30 op_sel_hi:[1,1,0]
	v_pk_fma_f16 v83, v71, v83, s30 op_sel_hi:[1,1,0]
	v_pk_fma_f16 v144, v72, v144, s30 op_sel_hi:[1,1,0]
	v_pk_fma_f16 v145, v73, v145, s30 op_sel_hi:[1,1,0]
	v_pk_fma_f16 v82, v70, v82, s31 op_sel_hi:[1,1,0]
	v_pk_fma_f16 v83, v71, v83, s31 op_sel_hi:[1,1,0]
	v_pk_fma_f16 v144, v72, v144, s31 op_sel_hi:[1,1,0]
	v_pk_fma_f16 v145, v73, v145, s31 op_sel_hi:[1,1,0]
	v_pk_fma_f16 v82, v70, v82, s41 op_sel_hi:[1,1,0]
	v_pk_fma_f16 v83, v71, v83, s41 op_sel_hi:[1,1,0]
	v_pk_fma_f16 v144, v72, v144, s41 op_sel_hi:[1,1,0]
	v_pk_fma_f16 v145, v73, v145, s41 op_sel_hi:[1,1,0]
	v_pk_max_f16 v68, v68, v228
	v_pk_max_f16 v69, v69, v228
	v_pk_fma_f16 v70, v70, v82, s42 op_sel_hi:[1,1,0]
	v_pk_fma_f16 v71, v71, v83, s42 op_sel_hi:[1,1,0]
	v_pk_fma_f16 v72, v72, v144, s42 op_sel_hi:[1,1,0]
	v_pk_fma_f16 v73, v73, v145, s42 op_sel_hi:[1,1,0]
	v_pk_add_f16 v66, v66, v70
	v_pk_add_f16 v67, v67, v71
	v_pk_add_f16 v68, v68, v72
	v_pk_add_f16 v69, v69, v73
	v_cvt_pk_f16_f32 v70, v74, v75
	v_cvt_pk_f16_f32 v71, v76, v77
	v_cvt_pk_f16_f32 v72, v78, v79
	v_cvt_pk_f16_f32 v73, v80, v81
	v_and_b32_e32 v74, 0x7fff7fff, v70
	v_and_b32_e32 v75, 0x7fff7fff, v71
	v_and_b32_e32 v76, 0x7fff7fff, v72
	v_and_b32_e32 v77, 0x7fff7fff, v73
	v_pk_min_f16 v74, v74, v229
	v_pk_min_f16 v75, v75, v229
	v_pk_min_f16 v76, v76, v229
	v_pk_min_f16 v77, v77, v229
	s_waitcnt lgkmcnt(7)
	v_mfma_f32_32x32x16_f16 v[2:17], v[190:193], v[66:69], v[2:17]
	v_pk_fma_f16 v74, v74, s26, -1.0 op_sel_hi:[1,0,0]
	v_pk_fma_f16 v75, v75, s26, -1.0 op_sel_hi:[1,0,0]
	v_pk_fma_f16 v76, v76, s26, -1.0 op_sel_hi:[1,0,0]
	v_pk_fma_f16 v77, v77, s26, -1.0 op_sel_hi:[1,0,0]
	v_pk_fma_f16 v78, v74, s27, v230 op_sel_hi:[1,0,0]
	v_pk_fma_f16 v79, v75, s27, v230 op_sel_hi:[1,0,0]
	v_pk_fma_f16 v80, v76, s27, v230 op_sel_hi:[1,0,0]
	v_pk_fma_f16 v81, v77, s27, v230 op_sel_hi:[1,0,0]
	s_waitcnt lgkmcnt(5)
	v_mfma_f32_32x32x16_f16 v[18:33], v[198:201], v[66:69], v[18:33]
	v_pk_fma_f16 v78, v74, v78, s28 op_sel_hi:[1,1,0]
	v_pk_fma_f16 v79, v75, v79, s28 op_sel_hi:[1,1,0]
	v_pk_fma_f16 v80, v76, v80, s28 op_sel_hi:[1,1,0]
	v_pk_fma_f16 v81, v77, v81, s28 op_sel_hi:[1,1,0]
	v_pk_fma_f16 v78, v74, v78, s29 op_sel_hi:[1,1,0]
	v_pk_fma_f16 v79, v75, v79, s29 op_sel_hi:[1,1,0]
	v_pk_fma_f16 v80, v76, v80, s29 op_sel_hi:[1,1,0]
	s_waitcnt lgkmcnt(3)
	v_mfma_f32_32x32x16_f16 v[34:49], v[212:215], v[66:69], v[34:49]
	v_pk_fma_f16 v81, v77, v81, s29 op_sel_hi:[1,1,0]
	v_pk_fma_f16 v78, v74, v78, s30 op_sel_hi:[1,1,0]
	v_pk_fma_f16 v79, v75, v79, s30 op_sel_hi:[1,1,0]
	v_pk_fma_f16 v80, v76, v80, s30 op_sel_hi:[1,1,0]
	v_pk_fma_f16 v81, v77, v81, s30 op_sel_hi:[1,1,0]
	v_pk_fma_f16 v78, v74, v78, s31 op_sel_hi:[1,1,0]
	v_pk_fma_f16 v79, v75, v79, s31 op_sel_hi:[1,1,0]
	s_waitcnt lgkmcnt(1)
	v_mfma_f32_32x32x16_f16 v[50:65], v[236:239], v[66:69], v[50:65]
	v_pk_fma_f16 v80, v76, v80, s31 op_sel_hi:[1,1,0]
	v_pk_fma_f16 v81, v77, v81, s31 op_sel_hi:[1,1,0]
	v_pk_fma_f16 v78, v74, v78, s41 op_sel_hi:[1,1,0]
	v_pk_fma_f16 v79, v75, v79, s41 op_sel_hi:[1,1,0]
	v_pk_fma_f16 v80, v76, v80, s41 op_sel_hi:[1,1,0]
	v_pk_fma_f16 v81, v77, v81, s41 op_sel_hi:[1,1,0]
	v_pk_max_f16 v70, v70, v228
	v_pk_max_f16 v71, v71, v228
	v_pk_max_f16 v72, v72, v228
	v_pk_max_f16 v73, v73, v228
	v_pk_fma_f16 v74, v74, v78, s42 op_sel_hi:[1,1,0]
	v_pk_fma_f16 v75, v75, v79, s42 op_sel_hi:[1,1,0]
	v_pk_fma_f16 v76, v76, v80, s42 op_sel_hi:[1,1,0]
	v_pk_fma_f16 v77, v77, v81, s42 op_sel_hi:[1,1,0]
	v_pk_add_f16 v70, v70, v74
	v_pk_add_f16 v71, v71, v75
	v_pk_add_f16 v72, v72, v76
	v_pk_add_f16 v73, v73, v77
	s_cmp_lg_u32 s16, 7
	s_nop 0
	v_mfma_f32_32x32x16_f16 v[2:17], v[194:197], v[70:73], v[2:17]
	v_mfma_f32_32x32x16_f16 v[18:33], v[202:205], v[70:73], v[18:33]
	v_mfma_f32_32x32x16_f16 v[34:49], v[232:235], v[70:73], v[34:49]
	s_waitcnt lgkmcnt(0)
	v_mfma_f32_32x32x16_f16 v[50:65], v[240:243], v[70:73], v[50:65]
	s_cbranch_scc1 .LBB1_25
	ds_read_b128 v[198:201], v231 offset:33280
	ds_read_b128 v[190:193], v231 offset:33312
	ds_read_b128 v[202:205], v231 offset:33792
	ds_read_b128 v[194:197], v231 offset:33824
	ds_read_b128 v[74:77], v231 offset:33344
	ds_read_b128 v[66:69], v231 offset:33376
	ds_read_b128 v[78:81], v231 offset:33856
	ds_read_b128 v[70:73], v231 offset:33888
	s_lshr_b32 s24, s40, 3
	s_cmp_lt_u32 s40, 16
	s_cselect_b64 s[16:17], -1, 0
	s_cmp_gt_u32 s40, 15
	s_cselect_b64 s[22:23], -1, 0
	s_and_saveexec_b64 s[18:19], s[8:9]
	s_xor_b64 s[18:19], exec, s[18:19]
	s_cbranch_execz .LBB1_41
	s_mov_b64 s[20:21], -1
	s_and_b64 vcc, exec, s[22:23]
	s_cbranch_vccz .LBB1_39
	s_cmp_eq_u32 s24, 2
	s_cselect_b32 s25, 2, -1
	s_mov_b64 s[20:21], 0
